# DeltaNet state step: packed f32 state scaling split into scalar multiplies
# speedup vs baseline: 1.0001x; 1.0001x over previous
.LBB0_1633:
	s_lshl_b32 s10, s50, 4
	s_bitcmp1_b32 s47, 0
	v_and_b32_e32 v2, 31, v68
	v_ashrrev_i32_e32 v177, 5, v68
	s_cselect_b32 s11, 0x11c00, 0
	v_add_u32_e32 v178, s11, v1
	v_mul_u32_u24_e32 v68, 0x110, v2
	v_lshlrev_b32_e32 v168, 3, v177
	v_add3_u32 v169, v178, v68, v168
	v_add_u32_e32 v100, 0x2000, v169
	ds_read2_b64 v[68:71], v169 offset1:2
	ds_read2_b64 v[72:75], v169 offset0:4 offset1:6
	ds_read2_b64 v[88:91], v100 offset0:64 offset1:66
	ds_read2_b64 v[92:95], v100 offset0:68 offset1:70
	ds_read2_b64 v[76:79], v169 offset0:8 offset1:10
	ds_read2_b64 v[96:99], v100 offset0:72 offset1:74
	ds_read2_b64 v[80:83], v169 offset0:12 offset1:14
	ds_read2_b64 v[116:119], v100 offset0:76 offset1:78
	ds_read2_b64 v[170:173], v169 offset0:16 offset1:18
	ds_read2_b64 v[180:183], v169 offset0:20 offset1:22
	ds_read2_b64 v[184:187], v100 offset0:80 offset1:82
	ds_read2_b64 v[188:191], v100 offset0:84 offset1:86
	ds_read2_b64 v[192:195], v169 offset0:24 offset1:26
	ds_read2_b64 v[196:199], v100 offset0:88 offset1:90
	ds_read2_b64 v[200:203], v169 offset0:28 offset1:30
	ds_read2_b64 v[204:207], v100 offset0:92 offset1:94
	v_cvt_pk_bf16_f32 v84, v52, v53
	v_cvt_pk_bf16_f32 v85, v54, v55
	v_cvt_pk_bf16_f32 v86, v56, v57
	v_cvt_pk_bf16_f32 v87, v58, v59
	v_cvt_pk_bf16_f32 v156, v60, v61
	v_cvt_pk_bf16_f32 v157, v62, v63
	v_cvt_pk_bf16_f32 v158, v64, v65
	v_cvt_pk_bf16_f32 v159, v66, v67
	v_cvt_pk_bf16_f32 v160, v36, v37
	v_cvt_pk_bf16_f32 v161, v38, v39
	v_cvt_pk_bf16_f32 v162, v40, v41
	v_cvt_pk_bf16_f32 v163, v42, v43
	v_cvt_pk_bf16_f32 v164, v44, v45
	v_cvt_pk_bf16_f32 v165, v46, v47
	v_cvt_pk_bf16_f32 v166, v48, v49
	v_cvt_pk_bf16_f32 v167, v50, v51
	v_cvt_pk_bf16_f32 v144, v20, v21
	v_cvt_pk_bf16_f32 v145, v22, v23
	v_cvt_pk_bf16_f32 v146, v24, v25
	v_cvt_pk_bf16_f32 v147, v26, v27
	v_cvt_pk_bf16_f32 v152, v28, v29
	v_cvt_pk_bf16_f32 v153, v30, v31
	v_cvt_pk_bf16_f32 v154, v32, v33
	v_cvt_pk_bf16_f32 v155, v34, v35
	v_cvt_pk_bf16_f32 v148, v4, v5
	v_cvt_pk_bf16_f32 v149, v6, v7
	v_cvt_pk_bf16_f32 v150, v8, v9
	v_cvt_pk_bf16_f32 v151, v10, v11
	v_cvt_pk_bf16_f32 v140, v12, v13
	v_cvt_pk_bf16_f32 v141, v14, v15
	v_cvt_pk_bf16_f32 v142, v16, v17
	v_cvt_pk_bf16_f32 v143, v18, v19
	s_or_b32 s10, s10, s42
	s_waitcnt lgkmcnt(13)
	v_mfma_f32_32x32x16_bf16 v[100:115], v[88:91], v[84:87], 0
	s_waitcnt lgkmcnt(12)
	v_mfma_f32_32x32x16_bf16 v[100:115], v[92:95], v[156:159], v[100:115]
	s_waitcnt lgkmcnt(10)
	v_mfma_f32_32x32x16_bf16 v[100:115], v[96:99], v[160:163], v[100:115]
	s_waitcnt lgkmcnt(8)
	v_mfma_f32_32x32x16_bf16 v[100:115], v[116:119], v[164:167], v[100:115]
	v_mfma_f32_32x32x16_bf16 v[116:131], v[68:71], v[84:87], 0
	v_mfma_f32_32x32x16_bf16 v[116:131], v[72:75], v[156:159], v[116:131]
	v_add_u32_e32 v72, 0x4000, v169
	v_add_u32_e32 v73, 0x6000, v169
	ds_read2_b64 v[88:91], v72 offset0:128 offset1:130
	ds_read2_b64 v[208:211], v72 offset0:132 offset1:134
	ds_read2_b64 v[68:71], v73 offset0:192 offset1:194
	ds_read2_b64 v[92:95], v73 offset0:196 offset1:198
	ds_read2_b64 v[212:215], v72 offset0:136 offset1:138
	ds_read2_b64 v[96:99], v73 offset0:200 offset1:202
	ds_read2_b64 v[216:219], v72 offset0:140 offset1:142
	ds_read2_b64 v[220:223], v73 offset0:204 offset1:206
	v_mfma_f32_32x32x16_bf16 v[116:131], v[76:79], v[160:163], v[116:131]
	v_mfma_f32_32x32x16_bf16 v[116:131], v[80:83], v[164:167], v[116:131]
	s_waitcnt lgkmcnt(13)
	v_mfma_f32_32x32x16_bf16 v[100:115], v[184:187], v[144:147], v[100:115]
	s_waitcnt lgkmcnt(12)
	v_mfma_f32_32x32x16_bf16 v[100:115], v[188:191], v[152:155], v[100:115]
	s_waitcnt lgkmcnt(10)
	v_mfma_f32_32x32x16_bf16 v[100:115], v[196:199], v[148:151], v[100:115]
	s_waitcnt lgkmcnt(8)
	v_mfma_f32_32x32x16_bf16 v[100:115], v[204:207], v[140:143], v[100:115]
	v_mfma_f32_32x32x16_bf16 v[116:131], v[170:173], v[144:147], v[116:131]
	ds_read2_b64 v[170:173], v72 offset0:144 offset1:146
	v_mfma_f32_32x32x16_bf16 v[116:131], v[180:183], v[152:155], v[116:131]
	v_mfma_f32_32x32x16_bf16 v[116:131], v[192:195], v[148:151], v[116:131]
	ds_read2_b64 v[180:183], v72 offset0:148 offset1:150
	ds_read2_b64 v[184:187], v73 offset0:208 offset1:210
	ds_read2_b64 v[188:191], v73 offset0:212 offset1:214
	ds_read2_b64 v[192:195], v72 offset0:152 offset1:154
	ds_read2_b64 v[196:199], v73 offset0:216 offset1:218
	ds_read2_b64 v[204:207], v72 offset0:156 offset1:158
	ds_read2_b64 v[224:227], v73 offset0:220 offset1:222
	v_mfma_f32_32x32x16_bf16 v[116:131], v[200:203], v[140:143], v[116:131]
	s_waitcnt lgkmcnt(13)
	v_mfma_f32_32x32x16_bf16 v[68:83], v[68:71], v[84:87], 0
	s_waitcnt lgkmcnt(12)
	v_mfma_f32_32x32x16_bf16 v[68:83], v[92:95], v[156:159], v[68:83]
	s_waitcnt lgkmcnt(10)
	v_mfma_f32_32x32x16_bf16 v[68:83], v[96:99], v[160:163], v[68:83]
	s_waitcnt lgkmcnt(8)
	v_mfma_f32_32x32x16_bf16 v[68:83], v[220:223], v[164:167], v[68:83]
	v_mfma_f32_32x32x16_bf16 v[84:99], v[88:91], v[84:87], 0
	v_mfma_f32_32x32x16_bf16 v[84:99], v[208:211], v[156:159], v[84:99]
	v_lshlrev_b32_e32 v156, 4, v177
	v_add3_u32 v156, v178, s41, v156
	v_mov_b32_e32 v159, 0x1200
	v_mad_u32_u24 v158, v2, s33, v156
	v_mad_u32_u24 v159, v2, s33, v159
	v_add_u32_e32 v156, v156, v159
	v_mul_u32_u24_e32 v157, 0x90, v2
	v_mfma_f32_32x32x16_bf16 v[84:99], v[212:215], v[160:163], v[84:99]
	ds_read_b128 v[200:203], v158 offset:63488
	ds_read_b128 v[208:211], v158 offset:63520
	ds_read_b128 v[212:215], v156 offset:63488
	ds_read_b128 v[220:223], v156 offset:63520
	v_mfma_f32_32x32x16_bf16 v[84:99], v[216:219], v[164:167], v[84:99]
	s_waitcnt lgkmcnt(11)
	v_mfma_f32_32x32x16_bf16 v[84:99], v[170:173], v[144:147], v[84:99]
	v_add3_u32 v179, v178, v157, v168
	v_add3_u32 v232, v178, v159, v168
	v_add_u32_e32 v156, 0xd000, v179
	v_add_u32_e32 v157, 0xd000, v232
	s_waitcnt lgkmcnt(10)
	v_mfma_f32_32x32x16_bf16 v[84:99], v[180:183], v[152:155], v[84:99]
	ds_read2_b64 v[180:183], v156 offset1:2
	ds_read2_b64 v[216:219], v156 offset0:4 offset1:6
	s_waitcnt lgkmcnt(9)
	v_mfma_f32_32x32x16_bf16 v[84:99], v[192:195], v[148:151], v[84:99]
	ds_read2_b64 v[168:171], v157 offset1:2
	ds_read2_b64 v[164:167], v157 offset0:4 offset1:6
	ds_read2_b64 v[192:195], v156 offset0:8 offset1:10
	ds_read2_b64 v[160:163], v157 offset0:8 offset1:10
	ds_read2_b64 v[228:231], v156 offset0:12 offset1:14
	ds_read2_b64 v[156:159], v157 offset0:12 offset1:14
	s_waitcnt lgkmcnt(13)
	v_mfma_f32_32x32x16_bf16 v[84:99], v[204:207], v[140:143], v[84:99]
	s_waitcnt lgkmcnt(11)
	v_mfma_f32_32x32x16_bf16 v[116:131], v[200:203], v[132:135], v[116:131]
	s_waitcnt lgkmcnt(9)
	v_mfma_f32_32x32x16_bf16 v[100:115], v[212:215], v[132:135], v[100:115]
	v_mfma_f32_32x32x16_bf16 v[68:83], v[184:187], v[144:147], v[68:83]
	v_mfma_f32_32x32x16_bf16 v[116:131], v[208:211], v[136:139], v[116:131]
	s_waitcnt lgkmcnt(8)
	v_mfma_f32_32x32x16_bf16 v[100:115], v[220:223], v[136:139], v[100:115]
	s_nop 9
	v_cvt_pk_bf16_f32 v172, v116, v117
	v_cvt_pk_bf16_f32 v173, v118, v119
	v_cvt_pk_bf16_f32 v174, v120, v121
	v_cvt_pk_bf16_f32 v175, v122, v123
	v_cvt_pk_bf16_f32 v120, v124, v125
	v_cvt_pk_bf16_f32 v121, v126, v127
	v_cvt_pk_bf16_f32 v122, v128, v129
	v_mfma_f32_32x32x16_bf16 v[68:83], v[188:191], v[152:155], v[68:83]
	v_cvt_pk_bf16_f32 v123, v130, v131
	v_cvt_pk_bf16_f32 v116, v100, v101
	v_cvt_pk_bf16_f32 v117, v102, v103
	v_cvt_pk_bf16_f32 v118, v104, v105
	v_cvt_pk_bf16_f32 v119, v106, v107
	v_cvt_pk_bf16_f32 v100, v108, v109
	v_cvt_pk_bf16_f32 v101, v110, v111
	v_cvt_pk_bf16_f32 v102, v112, v113
	v_cvt_pk_bf16_f32 v103, v114, v115
	v_mfma_f32_32x32x16_bf16 v[68:83], v[196:199], v[148:151], v[68:83]
	v_add_u32_e32 v184, 0x8800, v179
	v_add_u32_e32 v185, 0x8800, v232
	v_add_u32_e32 v190, 0xa800, v179
	v_add_u32_e32 v196, 0xb800, v179
	ds_read2_b64 v[108:111], v184 offset1:2
	ds_read2_b64 v[104:107], v184 offset0:4 offset1:6
	ds_read2_b64 v[124:127], v185 offset1:2
	ds_read2_b64 v[112:115], v185 offset0:4 offset1:6
	ds_read2_b64 v[128:131], v190 offset0:128 offset1:130
	ds_read2_b64 v[144:147], v196 offset0:192 offset1:194
	ds_read2_b64 v[148:151], v190 offset0:132 offset1:134
	ds_read2_b64 v[152:155], v196 offset0:196 offset1:198
	v_mfma_f32_32x32x16_bf16 v[68:83], v[224:227], v[140:143], v[68:83]
	s_waitcnt lgkmcnt(14)
	v_mfma_f32_32x32x16_bf16 v[84:99], v[180:183], v[172:175], v[84:99]
	ds_read_b32 v140, v178 offset:62976
	s_waitcnt lgkmcnt(0)
	v_mul_f32_e64 v66, v66, v140
	v_mul_f32_e64 v67, v67, v140
	v_mul_f32_e64 v64, v64, v140
	v_mul_f32_e64 v65, v65, v140
	v_mfma_f32_32x32x16_bf16 v[84:99], v[216:219], v[120:123], v[84:99]
	v_mul_f32_e64 v62, v62, v140
	v_mul_f32_e64 v63, v63, v140
	v_mul_f32_e64 v60, v60, v140
	v_mul_f32_e64 v61, v61, v140
	v_mul_f32_e64 v58, v58, v140
	v_mul_f32_e64 v59, v59, v140
	v_mul_f32_e64 v56, v56, v140
	v_mul_f32_e64 v57, v57, v140
	v_mul_f32_e64 v54, v54, v140
	v_mul_f32_e64 v55, v55, v140
	v_mul_f32_e64 v52, v52, v140
	v_mul_f32_e64 v53, v53, v140
	v_mul_f32_e64 v50, v50, v140
	v_mul_f32_e64 v51, v51, v140
	v_mfma_f32_32x32x16_bf16 v[84:99], v[192:195], v[116:119], v[84:99]
	v_mul_f32_e64 v48, v48, v140
	v_mul_f32_e64 v49, v49, v140
	v_mul_f32_e64 v46, v46, v140
	v_mul_f32_e64 v47, v47, v140
	v_mul_f32_e64 v44, v44, v140
	v_mul_f32_e64 v45, v45, v140
	v_mul_f32_e64 v42, v42, v140
	v_mul_f32_e64 v43, v43, v140
	v_mul_f32_e64 v40, v40, v140
	v_mul_f32_e64 v41, v41, v140
	v_mul_f32_e64 v38, v38, v140
	v_mul_f32_e64 v39, v39, v140
	v_mul_f32_e64 v36, v36, v140
	v_mul_f32_e64 v37, v37, v140
	v_mul_f32_e64 v34, v34, v140
	v_mul_f32_e64 v35, v35, v140
	v_mul_f32_e64 v32, v32, v140
	v_mul_f32_e64 v33, v33, v140
	v_mul_f32_e64 v30, v30, v140
	v_mul_f32_e64 v31, v31, v140
	v_mul_f32_e64 v28, v28, v140
	v_mul_f32_e64 v29, v29, v140
	v_mul_f32_e64 v26, v26, v140
	v_mul_f32_e64 v27, v27, v140
	v_mul_f32_e64 v24, v24, v140
	v_mul_f32_e64 v25, v25, v140
	v_mul_f32_e64 v22, v22, v140
	v_mul_f32_e64 v23, v23, v140
	v_mul_f32_e64 v20, v20, v140
	v_mul_f32_e64 v21, v21, v140
	v_mul_f32_e64 v18, v18, v140
	v_mul_f32_e64 v19, v19, v140
	v_mul_f32_e64 v16, v16, v140
	v_mul_f32_e64 v17, v17, v140
	v_mul_f32_e64 v14, v14, v140
	v_mul_f32_e64 v15, v15, v140
	v_mul_f32_e64 v12, v12, v140
	v_mul_f32_e64 v13, v13, v140
	v_mul_f32_e64 v10, v10, v140
	v_mul_f32_e64 v11, v11, v140
	v_mul_f32_e64 v8, v8, v140
	v_mul_f32_e64 v9, v9, v140
	v_mul_f32_e64 v6, v6, v140
	v_mul_f32_e64 v7, v7, v140
	v_mul_f32_e64 v4, v4, v140
	v_mul_f32_e64 v5, v5, v140
	v_mfma_f32_32x32x16_bf16 v[84:99], v[228:231], v[100:103], v[84:99]
	v_mfma_f32_32x32x16_bf16 v[68:83], v[168:171], v[172:175], v[68:83]
	ds_read2_b64 v[140:143], v184 offset0:8 offset1:10
	v_mfma_f32_32x32x16_bf16 v[68:83], v[164:167], v[120:123], v[68:83]
	ds_read2_b64 v[164:167], v184 offset0:12 offset1:14
	ds_read2_b64 v[168:171], v185 offset0:8 offset1:10
	ds_read2_b64 v[178:181], v185 offset0:12 offset1:14
	ds_read2_b64 v[182:185], v190 offset0:136 offset1:138
	ds_read2_b64 v[186:189], v196 offset0:200 offset1:202
	ds_read2_b64 v[190:193], v190 offset0:140 offset1:142
	ds_read2_b64 v[194:197], v196 offset0:204 offset1:206
	v_mfma_f32_32x32x16_bf16 v[68:83], v[160:163], v[116:119], v[68:83]
	v_mfma_f32_32x32x16_bf16 v[52:67], v[108:111], v[172:175], v[52:67]
	v_mfma_f32_32x32x16_bf16 v[36:51], v[124:127], v[172:175], v[36:51]
	v_mfma_f32_32x32x16_bf16 v[20:35], v[128:131], v[172:175], v[20:35]
	v_mfma_f32_32x32x16_bf16 v[4:19], v[144:147], v[172:175], v[4:19]
	v_mfma_f32_32x32x16_bf16 v[52:67], v[104:107], v[120:123], v[52:67]
	v_mfma_f32_32x32x16_bf16 v[36:51], v[112:115], v[120:123], v[36:51]
	v_mfma_f32_32x32x16_bf16 v[20:35], v[148:151], v[120:123], v[20:35]
	v_mfma_f32_32x32x16_bf16 v[4:19], v[152:155], v[120:123], v[4:19]
	s_ashr_i32 s11, s10, 31
	s_lshl_b64 s[10:11], s[10:11], 14
	s_add_u32 s10, s26, s10
	v_lshlrev_b32_e32 v104, 9, v177
	v_mfma_f32_32x32x16_bf16 v[68:83], v[156:159], v[100:103], v[68:83]
	s_addc_u32 s11, s27, s11
	v_ashrrev_i32_e32 v105, 31, v104
	v_lshl_add_u64 v[104:105], v[104:105], 1, s[10:11]
	v_lshl_add_u64 v[104:105], s[0:1], 1, v[104:105]
	v_lshlrev_b32_e32 v2, 1, v2
	v_lshl_add_u64 v[104:105], v[104:105], 0, v[2:3]
	s_movk_i32 s10, 0x2000
	v_add_co_u32_e32 v106, vcc, s10, v104
	s_movk_i32 s10, 0x3000
	s_nop 0
	v_addc_co_u32_e32 v107, vcc, 0, v105, vcc
	v_cvt_pk_bf16_f32 v2, v84, s0
	v_add_co_u32_e32 v108, vcc, s10, v104
	global_store_short v[104:105], v2, off
	v_cvt_pk_bf16_f32 v2, v68, s0
	v_addc_co_u32_e32 v109, vcc, 0, v105, vcc
	global_store_short v[108:109], v2, off offset:-4096
	v_cvt_pk_bf16_f32 v2, v85, s0
	global_store_short v[104:105], v2, off offset:256
	v_cvt_pk_bf16_f32 v2, v69, s0
	global_store_short v[106:107], v2, off offset:256
	v_cvt_pk_bf16_f32 v2, v86, s0
	global_store_short v[104:105], v2, off offset:512
	v_cvt_pk_bf16_f32 v2, v70, s0
	global_store_short v[106:107], v2, off offset:512
	v_cvt_pk_bf16_f32 v2, v87, s0
	global_store_short v[104:105], v2, off offset:768
	v_cvt_pk_bf16_f32 v2, v71, s0
	global_store_short v[106:107], v2, off offset:768
	v_cvt_pk_bf16_f32 v2, v88, s0
	global_store_short v[104:105], v2, off offset:2048
	v_cvt_pk_bf16_f32 v2, v72, s0
	global_store_short v[106:107], v2, off offset:2048
	v_cvt_pk_bf16_f32 v2, v89, s0
	global_store_short v[104:105], v2, off offset:2304
	v_cvt_pk_bf16_f32 v2, v73, s0
	global_store_short v[106:107], v2, off offset:2304
	v_cvt_pk_bf16_f32 v2, v90, s0
	global_store_short v[104:105], v2, off offset:2560
	v_cvt_pk_bf16_f32 v2, v74, s0
	global_store_short v[106:107], v2, off offset:2560
	v_cvt_pk_bf16_f32 v2, v91, s0
	s_movk_i32 s10, 0x1000
	global_store_short v[104:105], v2, off offset:2816
	v_cvt_pk_bf16_f32 v2, v75, s0
	v_add_co_u32_e32 v68, vcc, s10, v104
	global_store_short v[106:107], v2, off offset:2816
	v_cvt_pk_bf16_f32 v2, v92, s0
	v_addc_co_u32_e32 v69, vcc, 0, v105, vcc
	global_store_short v[68:69], v2, off
	v_cvt_pk_bf16_f32 v2, v76, s0
	global_store_short v[108:109], v2, off
	v_cvt_pk_bf16_f32 v2, v93, s0
	global_store_short v[68:69], v2, off offset:256
	v_cvt_pk_bf16_f32 v2, v77, s0
	s_waitcnt lgkmcnt(7)
	v_mfma_f32_32x32x16_bf16 v[52:67], v[140:143], v[116:119], v[52:67]
	global_store_short v[108:109], v2, off offset:256
	v_cvt_pk_bf16_f32 v2, v94, s0
	global_store_short v[68:69], v2, off offset:512
	v_cvt_pk_bf16_f32 v2, v78, s0
	global_store_short v[108:109], v2, off offset:512
	v_cvt_pk_bf16_f32 v2, v95, s0
	global_store_short v[68:69], v2, off offset:768
	s_waitcnt lgkmcnt(5)
	v_mfma_f32_32x32x16_bf16 v[36:51], v[168:171], v[116:119], v[36:51]
	v_cvt_pk_bf16_f32 v2, v79, s0
	global_store_short v[108:109], v2, off offset:768
	v_cvt_pk_bf16_f32 v2, v96, s0
	global_store_short v[68:69], v2, off offset:2048
	v_cvt_pk_bf16_f32 v2, v80, s0
	global_store_short v[108:109], v2, off offset:2048
	v_cvt_pk_bf16_f32 v2, v97, s0
	s_waitcnt lgkmcnt(3)
	v_mfma_f32_32x32x16_bf16 v[20:35], v[182:185], v[116:119], v[20:35]
	global_store_short v[68:69], v2, off offset:2304
	v_cvt_pk_bf16_f32 v2, v81, s0
	global_store_short v[108:109], v2, off offset:2304
	v_cvt_pk_bf16_f32 v2, v98, s0
	global_store_short v[68:69], v2, off offset:2560
	v_cvt_pk_bf16_f32 v2, v82, s0
	global_store_short v[108:109], v2, off offset:2560
	s_waitcnt lgkmcnt(2)
	v_mfma_f32_32x32x16_bf16 v[4:19], v[186:189], v[116:119], v[4:19]
	v_cvt_pk_bf16_f32 v2, v99, s0
	global_store_short v[68:69], v2, off offset:2816
	v_cvt_pk_bf16_f32 v2, v83, s0
	global_store_short v[108:109], v2, off offset:2816
	s_waitcnt lgkmcnt(0)
	s_barrier
	s_add_i32 s43, s43, -1
	s_add_i32 s46, s46, 1
	v_mfma_f32_32x32x16_bf16 v[52:67], v[164:167], v[100:103], v[52:67]
	s_cmp_lg_u32 s43, -1
	v_mfma_f32_32x32x16_bf16 v[36:51], v[178:181], v[100:103], v[36:51]
	s_waitcnt lgkmcnt(1)
	v_mfma_f32_32x32x16_bf16 v[20:35], v[190:193], v[100:103], v[20:35]
	s_waitcnt lgkmcnt(0)
	v_mfma_f32_32x32x16_bf16 v[4:19], v[194:197], v[100:103], v[4:19]
	s_cbranch_scc0 .LBB0_1638
